# mlstm_out2 output stage de-waterfalled: 8 gain-vector loads hoisted to block top, single vmcnt wait (strategy 7.1), on top of v3_epi
# speedup vs baseline: 1.0014x; 1.0011x over previous
.LBB0_1142:
	s_or_b64 exec, exec, s[2:3]
	v_lshl_add_u64 v[174:175], v[164:165], 2, v[158:159]
	global_load_dwordx4 v[92:95], v[174:175], off
	global_load_dwordx4 v[96:99], v[174:175], off offset:128
	global_load_dwordx4 v[170:173], v[174:175], off offset:32
	global_load_dwordx4 v[220:223], v[174:175], off offset:160
	global_load_dwordx4 v[224:227], v[174:175], off offset:64
	global_load_dwordx4 v[228:231], v[174:175], off offset:192
	global_load_dwordx4 v[232:235], v[174:175], off offset:96
	global_load_dwordx2 v[168:169], v[174:175], off offset:224
	global_load_dwordx2 v[176:177], v[174:175], off offset:232
	v_add_f32_e32 v70, v123, v129
	v_mul_f32_e32 v68, 0xbfb8aa3b, v70
	s_mov_b32 s2, 0xbfb8aa3b
	v_fma_f32 v69, v70, s2, -v68
	v_rndne_f32_e32 v71, v68
	v_fmac_f32_e32 v69, 0xb2a5705f, v70
	v_sub_f32_e32 v68, v68, v71
	v_add_f32_e32 v68, v68, v69
	v_exp_f32_e32 v72, v68
	v_cvt_i32_f32_e32 v71, v71
	v_pk_add_f32 v[68:69], v[116:117], v[118:119]
	s_mov_b32 s3, 0x42ce8ed0
	v_fmac_f32_e32 v69, v2, v68
	v_ldexp_f32 v2, v72, v71
	v_cmp_nlt_f32_e32 vcc, s3, v70
	s_mov_b32 s7, 0xc2b17218
	v_mov_b32_e32 v125, v121
	v_cndmask_b32_e32 v2, 0, v2, vcc
	v_cmp_ngt_f32_e32 vcc, s7, v70
	v_permlane32_swap_b32_e32 v121, v125
	s_nop 0
	v_cndmask_b32_e32 v2, v210, v2, vcc
	v_max_f32_e64 v2, |v69|, v2
	v_div_scale_f32 v68, s[0:1], v2, v2, 1.0
	v_rcp_f32_e32 v69, v68
	v_mov_b32_e32 v163, v3
	v_fma_f32 v70, -v68, v69, 1.0
	v_fmac_f32_e32 v69, v70, v69
	v_div_scale_f32 v70, vcc, 1.0, v2, 1.0
	v_mul_f32_e32 v71, v70, v69
	v_fma_f32 v72, -v68, v71, v70
	v_fmac_f32_e32 v71, v72, v69
	v_fma_f32 v68, -v68, v71, v70
	v_div_fmas_f32 v68, v68, v69, v71
	v_div_fixup_f32 v2, v68, v2, 1.0
	v_pk_fma_f32 v[70:71], v[4:5], v[2:3], 0 op_sel_hi:[1,0,0]
	ds_read_b32 v4, v200
	v_pk_fma_f32 v[74:75], v[6:7], v[2:3], 0 op_sel_hi:[1,0,0]
	v_pk_fma_f32 v[78:79], v[8:9], v[2:3], 0 op_sel_hi:[1,0,0]
	v_pk_fma_f32 v[80:81], v[24:25], v[2:3], 0 op_sel_hi:[1,0,0]
	v_pk_fma_f32 v[24:25], v[10:11], v[2:3], 0 op_sel_hi:[1,0,0]
	s_waitcnt lgkmcnt(0)
	v_add_f32_e32 v6, v128, v4
	v_mul_f32_e32 v4, 0xbfb8aa3b, v6
	v_fma_f32 v5, v6, s2, -v4
	v_rndne_f32_e32 v7, v4
	v_fmac_f32_e32 v5, 0xb2a5705f, v6
	v_sub_f32_e32 v4, v4, v7
	v_add_f32_e32 v4, v4, v5
	v_exp_f32_e32 v8, v4
	v_cvt_i32_f32_e32 v7, v7
	v_pk_add_f32 v[4:5], v[120:121], v[124:125]
	v_cmp_nlt_f32_e32 vcc, s3, v6
	v_fmac_f32_e32 v5, v122, v4
	v_ldexp_f32 v4, v8, v7
	v_cndmask_b32_e32 v4, 0, v4, vcc
	v_cmp_ngt_f32_e32 vcc, s7, v6
	v_pk_fma_f32 v[72:73], v[20:21], v[2:3], 0 op_sel_hi:[1,0,0]
	v_pk_fma_f32 v[76:77], v[22:23], v[2:3], 0 op_sel_hi:[1,0,0]
	v_cndmask_b32_e32 v4, v210, v4, vcc
	v_max_f32_e64 v8, |v5|, v4
	v_div_scale_f32 v9, s[0:1], v8, v8, 1.0
	v_rcp_f32_e32 v10, v9
	v_pk_fma_f32 v[26:27], v[26:27], v[2:3], 0 op_sel_hi:[1,0,0]
	v_pk_fma_f32 v[68:69], v[12:13], v[2:3], 0 op_sel_hi:[1,0,0]
	v_pk_fma_f32 v[20:21], v[28:29], v[2:3], 0 op_sel_hi:[1,0,0]
	v_pk_fma_f32 v[82:83], v[14:15], v[2:3], 0 op_sel_hi:[1,0,0]
	v_pk_fma_f32 v[22:23], v[30:31], v[2:3], 0 op_sel_hi:[1,0,0]
	v_pk_fma_f32 v[16:17], v[16:17], v[2:3], 0 op_sel_hi:[1,0,0]
	v_pk_fma_f32 v[14:15], v[32:33], v[2:3], 0 op_sel_hi:[1,0,0]
	v_pk_fma_f32 v[4:5], v[18:19], v[2:3], 0 op_sel_hi:[1,0,0]
	v_pk_fma_f32 v[6:7], v[34:35], v[2:3], 0 op_sel_hi:[1,0,0]
	v_fma_f32 v2, -v9, v10, 1.0
	v_fmac_f32_e32 v10, v2, v10
	v_div_scale_f32 v2, vcc, 1.0, v8, 1.0
	v_mul_f32_e32 v11, v2, v10
	v_fma_f32 v12, -v9, v11, v2
	v_fmac_f32_e32 v11, v12, v10
	v_fma_f32 v2, -v9, v11, v2
	v_div_fmas_f32 v2, v2, v10, v11
	v_div_fixup_f32 v2, v2, v8, 1.0
	v_pk_fma_f32 v[8:9], v[66:67], v[2:3], v[6:7] op_sel_hi:[1,0,1]
	v_pk_fma_f32 v[10:11], v[50:51], v[2:3], v[4:5] op_sel_hi:[1,0,1]
	v_pk_mul_f32 v[4:5], v[8:9], v[8:9]
	v_pk_fma_f32 v[18:19], v[10:11], v[10:11], v[4:5]
	s_waitcnt vmcnt(0)
	v_lshlrev_b32_e32 v30, 16, v114
	v_and_b32_e32 v31, 0xffff0000, v114
	v_mul_f32_e32 v30, 0xbfb8aa3b, v30
	v_exp_f32_e32 v30, v30
	v_mul_f32_e32 v31, 0xbfb8aa3b, v31
	v_exp_f32_e32 v31, v31
	v_lshlrev_b32_e32 v32, 16, v115
	v_add_f32_e32 v30, 1.0, v30
	v_rcp_f32_e32 v34, v30
	v_add_f32_e32 v30, 1.0, v31
	v_mul_f32_e32 v31, 0xbfb8aa3b, v32
	v_and_b32_e32 v33, 0xffff0000, v115
	v_exp_f32_e32 v31, v31
	v_mul_f32_e32 v32, 0xbfb8aa3b, v33
	v_exp_f32_e32 v32, v32
	v_rcp_f32_e32 v35, v30
	v_add_f32_e32 v30, 1.0, v31
	v_pk_fma_f32 v[52:53], v[52:53], v[2:3], v[72:73] op_sel_hi:[1,0,1]
	v_rcp_f32_e32 v50, v30
	v_pk_fma_f32 v[70:71], v[36:37], v[2:3], v[70:71] op_sel_hi:[1,0,1]
	v_pk_fma_f32 v[30:31], v[54:55], v[2:3], v[76:77] op_sel_hi:[1,0,1]
	v_pk_mul_f32 v[36:37], v[52:53], v[52:53]
	v_add_f32_e32 v51, 1.0, v32
	v_pk_fma_f32 v[66:67], v[38:39], v[2:3], v[74:75] op_sel_hi:[1,0,1]
	v_pk_mul_f32 v[32:33], v[30:31], v[30:31]
	v_pk_fma_f32 v[36:37], v[70:71], v[70:71], v[36:37]
	v_pk_fma_f32 v[32:33], v[66:67], v[66:67], v[32:33]
	v_pk_add_f32 v[36:37], v[36:37], v[36:37] op_sel:[0,1] op_sel_hi:[1,0]
	v_pk_fma_f32 v[38:39], v[56:57], v[2:3], v[80:81] op_sel_hi:[1,0,1]
	v_pk_add_f32 v[36:37], v[32:33], v[36:37]
	v_pk_fma_f32 v[54:55], v[40:41], v[2:3], v[78:79] op_sel_hi:[1,0,1]
	v_pk_mul_f32 v[40:41], v[38:39], v[38:39]
	v_pk_add_f32 v[36:37], v[32:33], v[36:37] op_sel:[1,0] op_sel_hi:[0,1]
	v_pk_fma_f32 v[32:33], v[42:43], v[2:3], v[24:25] op_sel_hi:[1,0,1]
	v_pk_fma_f32 v[24:25], v[58:59], v[2:3], v[26:27] op_sel_hi:[1,0,1]
	v_pk_fma_f32 v[40:41], v[54:55], v[54:55], v[40:41]
	v_pk_mul_f32 v[26:27], v[24:25], v[24:25]
	v_pk_add_f32 v[36:37], v[40:41], v[36:37]
	v_pk_fma_f32 v[26:27], v[32:33], v[32:33], v[26:27]
	v_pk_add_f32 v[36:37], v[40:41], v[36:37] op_sel:[1,0] op_sel_hi:[0,1]
	v_pk_add_f32 v[36:37], v[26:27], v[36:37]
	v_pk_fma_f32 v[20:21], v[60:61], v[2:3], v[20:21] op_sel_hi:[1,0,1]
	v_pk_add_f32 v[40:41], v[26:27], v[36:37] op_sel:[1,0] op_sel_hi:[0,1]
	v_pk_fma_f32 v[36:37], v[44:45], v[2:3], v[68:69] op_sel_hi:[1,0,1]
	v_pk_mul_f32 v[44:45], v[20:21], v[20:21]
	v_pk_fma_f32 v[22:23], v[62:63], v[2:3], v[22:23] op_sel_hi:[1,0,1]
	v_pk_fma_f32 v[44:45], v[36:37], v[36:37], v[44:45]
	v_pk_fma_f32 v[26:27], v[46:47], v[2:3], v[82:83] op_sel_hi:[1,0,1]
	v_pk_mul_f32 v[42:43], v[22:23], v[22:23]
	v_pk_add_f32 v[40:41], v[44:45], v[40:41]
	v_pk_fma_f32 v[42:43], v[26:27], v[26:27], v[42:43]
	v_pk_add_f32 v[40:41], v[44:45], v[40:41] op_sel:[1,0] op_sel_hi:[0,1]
	v_pk_add_f32 v[40:41], v[42:43], v[40:41]
	v_pk_fma_f32 v[14:15], v[64:65], v[2:3], v[14:15] op_sel_hi:[1,0,1]
	v_pk_add_f32 v[40:41], v[42:43], v[40:41] op_sel:[1,0] op_sel_hi:[0,1]
	v_pk_fma_f32 v[16:17], v[48:49], v[2:3], v[16:17] op_sel_hi:[1,0,1]
	v_pk_mul_f32 v[42:43], v[14:15], v[14:15]
	v_lshlrev_b64 v[28:29], 11, v[166:167]
	v_pk_fma_f32 v[42:43], v[16:17], v[16:17], v[42:43]
	v_lshl_add_u64 v[28:29], s[66:67], 0, v[28:29]
	v_pk_add_f32 v[40:41], v[42:43], v[40:41]
	v_lshl_add_u64 v[28:29], v[164:165], 1, v[28:29]
	v_pk_add_f32 v[40:41], v[42:43], v[40:41] op_sel:[1,0] op_sel_hi:[0,1]
	v_pk_add_f32 v[40:41], v[18:19], v[40:41]
	v_rcp_f32_e32 v51, v51
	v_pk_add_f32 v[18:19], v[18:19], v[40:41] op_sel:[1,0] op_sel_hi:[0,1]
	v_mov_b32_e32 v2, v18
	s_nop 1
	v_permlane32_swap_b32_e32 v18, v2
	v_add_f32_e32 v2, v18, v2
	v_fmamk_f32 v2, v2, 0x3c800000, v180
	v_mul_f32_e32 v18, 0x4b800000, v2
	v_cmp_gt_f32_e32 vcc, s33, v2
	s_mov_b32 s0, 0x1701b000
	s_nop 0
	v_cndmask_b32_e32 v2, v2, v18, vcc
	v_rsq_f32_e32 v2, v2
	v_lshl_add_u64 v[18:19], v[28:29], 0, v[162:163]
	v_mul_f32_e32 v28, 0x45800000, v2
	v_cndmask_b32_e32 v2, v2, v28, vcc
	v_pk_mul_f32 v[28:29], v[70:71], v[2:3] op_sel_hi:[1,0]
	v_pk_mul_f32 v[32:33], v[32:33], v[2:3] op_sel_hi:[1,0]
	v_pk_mul_f32 v[4:5], v[92:93], v[28:29]
	v_pk_mul_f32 v[28:29], v[66:67], v[2:3] op_sel_hi:[1,0]
	v_pk_mul_f32 v[4:5], v[34:35], v[4:5]
	v_pk_mul_f32 v[6:7], v[94:95], v[28:29]
	v_cvt_pk_bf16_f32 v4, v4, v5
	v_pk_mul_f32 v[6:7], v[50:51], v[6:7]
	v_pk_mul_f32 v[28:29], v[52:53], v[2:3] op_sel_hi:[1,0]
	v_cvt_pk_bf16_f32 v5, v6, v7
	v_add_co_u32_e32 v6, vcc, s0, v18
	s_mov_b64 s[0:1], 0x1701b200
	s_nop 0
	v_addc_co_u32_e32 v7, vcc, 0, v19, vcc
	global_store_dwordx2 v[6:7], v[4:5], off offset:512
	v_lshlrev_b32_e32 v6, 16, v112
	v_and_b32_e32 v7, 0xffff0000, v112
	v_mul_f32_e32 v6, 0xbfb8aa3b, v6
	v_mul_f32_e32 v7, 0xbfb8aa3b, v7
	v_lshl_add_u64 v[4:5], v[18:19], 0, s[0:1]
	v_lshlrev_b32_e32 v18, 16, v113
	v_exp_f32_e32 v6, v6
	v_exp_f32_e32 v7, v7
	v_and_b32_e32 v19, 0xffff0000, v113
	v_mul_f32_e32 v18, 0xbfb8aa3b, v18
	v_mul_f32_e32 v19, 0xbfb8aa3b, v19
	v_exp_f32_e32 v18, v18
	v_exp_f32_e32 v19, v19
	v_add_f32_e32 v6, 1.0, v6
	v_add_f32_e32 v7, 1.0, v7
	v_rcp_f32_e32 v6, v6
	v_rcp_f32_e32 v7, v7
	v_add_f32_e32 v18, 1.0, v18
	v_add_f32_e32 v19, 1.0, v19
	v_rcp_f32_e32 v18, v18
	v_rcp_f32_e32 v19, v19
	v_pk_mul_f32 v[34:35], v[54:55], v[2:3] op_sel_hi:[1,0]
	v_pk_mul_f32 v[24:25], v[24:25], v[2:3] op_sel_hi:[1,0]
	v_pk_mul_f32 v[26:27], v[26:27], v[2:3] op_sel_hi:[1,0]
	v_pk_mul_f32 v[20:21], v[20:21], v[2:3] op_sel_hi:[1,0]
	v_pk_mul_f32 v[22:23], v[22:23], v[2:3] op_sel_hi:[1,0]
	v_pk_mul_f32 v[16:17], v[16:17], v[2:3] op_sel_hi:[1,0]
	v_pk_mul_f32 v[10:11], v[10:11], v[2:3] op_sel_hi:[1,0]
	v_pk_mul_f32 v[14:15], v[14:15], v[2:3] op_sel_hi:[1,0]
	v_pk_mul_f32 v[8:9], v[8:9], v[2:3] op_sel_hi:[1,0]
	s_mov_b32 s0, s21
	v_pk_mul_f32 v[28:29], v[96:97], v[28:29]
	s_nop 0
	v_pk_mul_f32 v[6:7], v[6:7], v[28:29]
	v_pk_mul_f32 v[28:29], v[30:31], v[2:3] op_sel_hi:[1,0]
	v_cvt_pk_bf16_f32 v6, v6, v7
	v_pk_mul_f32 v[28:29], v[98:99], v[28:29]
	s_nop 0
	v_pk_mul_f32 v[18:19], v[18:19], v[28:29]
	s_nop 0
	v_cvt_pk_bf16_f32 v7, v18, v19
	global_store_dwordx2 v[4:5], v[6:7], off offset:64
	v_lshlrev_b32_e32 v6, 16, v110
	v_and_b32_e32 v7, 0xffff0000, v110
	v_lshlrev_b32_e32 v18, 16, v111
	v_and_b32_e32 v19, 0xffff0000, v111
	v_mul_f32_e32 v6, 0xbfb8aa3b, v6
	v_mul_f32_e32 v7, 0xbfb8aa3b, v7
	v_mul_f32_e32 v18, 0xbfb8aa3b, v18
	v_mul_f32_e32 v19, 0xbfb8aa3b, v19
	v_exp_f32_e32 v6, v6
	v_exp_f32_e32 v7, v7
	v_exp_f32_e32 v18, v18
	v_exp_f32_e32 v19, v19
	v_add_f32_e32 v6, 1.0, v6
	v_add_f32_e32 v7, 1.0, v7
	v_add_f32_e32 v18, 1.0, v18
	v_add_f32_e32 v19, 1.0, v19
	v_rcp_f32_e32 v6, v6
	v_rcp_f32_e32 v7, v7
	v_rcp_f32_e32 v18, v18
	v_rcp_f32_e32 v19, v19
	v_pk_mul_f32 v[28:29], v[34:35], v[170:171]
	v_pk_mul_f32 v[30:31], v[32:33], v[172:173]
	v_pk_mul_f32 v[6:7], v[6:7], v[28:29]
	v_pk_mul_f32 v[18:19], v[18:19], v[30:31]
	v_cvt_pk_bf16_f32 v6, v6, v7
	v_cvt_pk_bf16_f32 v7, v18, v19
	global_store_dwordx2 v[4:5], v[6:7], off offset:16
	v_lshlrev_b32_e32 v6, 16, v108
	v_and_b32_e32 v7, 0xffff0000, v108
	v_lshlrev_b32_e32 v18, 16, v109
	v_and_b32_e32 v19, 0xffff0000, v109
	v_mul_f32_e32 v6, 0xbfb8aa3b, v6
	v_mul_f32_e32 v7, 0xbfb8aa3b, v7
	v_mul_f32_e32 v18, 0xbfb8aa3b, v18
	v_mul_f32_e32 v19, 0xbfb8aa3b, v19
	v_exp_f32_e32 v6, v6
	v_exp_f32_e32 v7, v7
	v_exp_f32_e32 v18, v18
	v_exp_f32_e32 v19, v19
	v_add_f32_e32 v6, 1.0, v6
	v_add_f32_e32 v7, 1.0, v7
	v_add_f32_e32 v18, 1.0, v18
	v_add_f32_e32 v19, 1.0, v19
	v_rcp_f32_e32 v6, v6
	v_rcp_f32_e32 v7, v7
	v_rcp_f32_e32 v18, v18
	v_rcp_f32_e32 v19, v19
	v_pk_mul_f32 v[32:33], v[38:39], v[2:3] op_sel_hi:[1,0]
	v_pk_mul_f32 v[24:25], v[24:25], v[222:223]
	v_pk_mul_f32 v[28:29], v[32:33], v[220:221]
	v_pk_mul_f32 v[18:19], v[18:19], v[24:25]
	v_pk_mul_f32 v[6:7], v[6:7], v[28:29]
	v_pk_mul_f32 v[24:25], v[36:37], v[2:3] op_sel_hi:[1,0]
	v_cvt_pk_bf16_f32 v6, v6, v7
	v_cvt_pk_bf16_f32 v7, v18, v19
	global_store_dwordx2 v[4:5], v[6:7], off offset:80
	v_lshlrev_b32_e32 v6, 16, v106
	v_and_b32_e32 v7, 0xffff0000, v106
	v_lshlrev_b32_e32 v18, 16, v107
	v_and_b32_e32 v19, 0xffff0000, v107
	v_mul_f32_e32 v6, 0xbfb8aa3b, v6
	v_mul_f32_e32 v7, 0xbfb8aa3b, v7
	v_mul_f32_e32 v18, 0xbfb8aa3b, v18
	v_mul_f32_e32 v19, 0xbfb8aa3b, v19
	v_exp_f32_e32 v6, v6
	v_exp_f32_e32 v7, v7
	v_exp_f32_e32 v18, v18
	v_exp_f32_e32 v19, v19
	v_add_f32_e32 v6, 1.0, v6
	v_add_f32_e32 v7, 1.0, v7
	v_add_f32_e32 v18, 1.0, v18
	v_add_f32_e32 v19, 1.0, v19
	v_rcp_f32_e32 v6, v6
	v_rcp_f32_e32 v7, v7
	v_rcp_f32_e32 v18, v18
	v_rcp_f32_e32 v19, v19
	v_pk_mul_f32 v[24:25], v[24:25], v[224:225]
	v_pk_mul_f32 v[26:27], v[26:27], v[226:227]
	v_pk_mul_f32 v[6:7], v[6:7], v[24:25]
	v_pk_mul_f32 v[18:19], v[18:19], v[26:27]
	v_cvt_pk_bf16_f32 v6, v6, v7
	v_cvt_pk_bf16_f32 v7, v18, v19
	global_store_dwordx2 v[4:5], v[6:7], off offset:32
	v_lshlrev_b32_e32 v6, 16, v104
	v_and_b32_e32 v7, 0xffff0000, v104
	v_lshlrev_b32_e32 v18, 16, v105
	v_and_b32_e32 v19, 0xffff0000, v105
	v_mul_f32_e32 v6, 0xbfb8aa3b, v6
	v_mul_f32_e32 v7, 0xbfb8aa3b, v7
	v_mul_f32_e32 v18, 0xbfb8aa3b, v18
	v_mul_f32_e32 v19, 0xbfb8aa3b, v19
	v_exp_f32_e32 v6, v6
	v_exp_f32_e32 v7, v7
	v_exp_f32_e32 v18, v18
	v_exp_f32_e32 v19, v19
	v_add_f32_e32 v6, 1.0, v6
	v_add_f32_e32 v7, 1.0, v7
	v_add_f32_e32 v18, 1.0, v18
	v_add_f32_e32 v19, 1.0, v19
	v_rcp_f32_e32 v6, v6
	v_rcp_f32_e32 v7, v7
	v_rcp_f32_e32 v18, v18
	v_rcp_f32_e32 v19, v19
	v_pk_mul_f32 v[20:21], v[20:21], v[228:229]
	v_pk_mul_f32 v[22:23], v[22:23], v[230:231]
	v_pk_mul_f32 v[6:7], v[6:7], v[20:21]
	v_pk_mul_f32 v[18:19], v[18:19], v[22:23]
	v_cvt_pk_bf16_f32 v6, v6, v7
	v_cvt_pk_bf16_f32 v7, v18, v19
	global_store_dwordx2 v[4:5], v[6:7], off offset:96
	v_lshlrev_b32_e32 v6, 16, v102
	v_and_b32_e32 v7, 0xffff0000, v102
	v_lshlrev_b32_e32 v22, 16, v103
	v_and_b32_e32 v23, 0xffff0000, v103
	v_mul_f32_e32 v6, 0xbfb8aa3b, v6
	v_mul_f32_e32 v7, 0xbfb8aa3b, v7
	v_mul_f32_e32 v22, 0xbfb8aa3b, v22
	v_mul_f32_e32 v23, 0xbfb8aa3b, v23
	v_exp_f32_e32 v6, v6
	v_exp_f32_e32 v7, v7
	v_exp_f32_e32 v22, v22
	v_exp_f32_e32 v23, v23
	v_add_f32_e32 v6, 1.0, v6
	v_add_f32_e32 v7, 1.0, v7
	v_add_f32_e32 v22, 1.0, v22
	v_add_f32_e32 v23, 1.0, v23
	v_rcp_f32_e32 v6, v6
	v_rcp_f32_e32 v7, v7
	v_rcp_f32_e32 v22, v22
	v_rcp_f32_e32 v23, v23
	v_pk_mul_f32 v[16:17], v[16:17], v[232:233]
	v_pk_mul_f32 v[10:11], v[10:11], v[234:235]
	v_pk_mul_f32 v[6:7], v[6:7], v[16:17]
	v_pk_mul_f32 v[10:11], v[22:23], v[10:11]
	v_cvt_pk_bf16_f32 v6, v6, v7
	v_cvt_pk_bf16_f32 v7, v10, v11
	global_store_dwordx2 v[4:5], v[6:7], off offset:48
	v_lshlrev_b32_e32 v6, 16, v100
	v_and_b32_e32 v7, 0xffff0000, v100
	v_lshlrev_b32_e32 v16, 16, v101
	v_and_b32_e32 v17, 0xffff0000, v101
	v_mul_f32_e32 v6, 0xbfb8aa3b, v6
	v_mul_f32_e32 v7, 0xbfb8aa3b, v7
	v_mul_f32_e32 v16, 0xbfb8aa3b, v16
	v_mul_f32_e32 v17, 0xbfb8aa3b, v17
	v_exp_f32_e32 v6, v6
	v_exp_f32_e32 v7, v7
	v_exp_f32_e32 v16, v16
	v_exp_f32_e32 v17, v17
	v_add_f32_e32 v6, 1.0, v6
	v_add_f32_e32 v7, 1.0, v7
	v_add_f32_e32 v16, 1.0, v16
	v_add_f32_e32 v17, 1.0, v17
	v_rcp_f32_e32 v6, v6
	v_rcp_f32_e32 v7, v7
	v_rcp_f32_e32 v16, v16
	v_rcp_f32_e32 v17, v17
	v_pk_mul_f32 v[10:11], v[14:15], v[168:169]
	v_pk_mul_f32 v[8:9], v[8:9], v[176:177]
	v_pk_mul_f32 v[6:7], v[6:7], v[10:11]
	v_pk_mul_f32 v[8:9], v[16:17], v[8:9]
	v_cvt_pk_bf16_f32 v6, v6, v7
	v_cvt_pk_bf16_f32 v7, v8, v9
	global_store_dwordx2 v[4:5], v[6:7], off offset:112
	s_barrier
	s_add_i32 s15, s0, s15
	s_lshl_b32 s7, s15, 1
	s_cmp_lt_i32 s7, s14
	s_cbranch_scc0 .LBB0_1242
